# 64-byte alignment of the four GEMM K-loop heads
# baseline (speedup 1.0000x reference)
.LBB0_156:
	s_ashr_i32 s31, s30, 31
	s_lshl_b64 s[34:35], s[30:31], 20
	s_add_u32 s34, s1, s34
	s_addc_u32 s35, s15, s35
	s_and_b64 s[36:37], s[2:3], exec
	s_cselect_b32 s31, s35, s43
	s_cselect_b32 s39, s34, s42
	s_ashr_i32 s29, s28, 31
	s_lshl_b64 s[36:37], s[28:29], 20
	s_add_u32 s36, s17, s36
	s_addc_u32 s37, s19, s37
	s_and_b64 s[46:47], s[2:3], exec
	s_cselect_b32 s29, s37, s45
	s_cselect_b32 s70, s36, s44
	s_add_u32 s42, s42, 0x80
	s_addc_u32 s43, s43, 0
	s_add_u32 s71, s44, 0x100
	v_mov_b32_e32 v34, 0
	s_addc_u32 s72, s45, 0
	s_mov_b32 s73, -2
	v_mov_b32_e32 v35, v34
	v_mov_b32_e32 v36, v34
	v_mov_b32_e32 v37, v34
	v_mov_b32_e32 v38, v34
	v_mov_b32_e32 v39, v34
	v_mov_b32_e32 v40, v34
	v_mov_b32_e32 v41, v34
	v_mov_b32_e32 v50, v34
	v_mov_b32_e32 v51, v34
	v_mov_b32_e32 v52, v34
	v_mov_b32_e32 v53, v34
	v_mov_b32_e32 v54, v34
	v_mov_b32_e32 v55, v34
	v_mov_b32_e32 v56, v34
	v_mov_b32_e32 v57, v34
	v_mov_b32_e32 v10, v34
	v_mov_b32_e32 v11, v34
	v_mov_b32_e32 v12, v34
	v_mov_b32_e32 v13, v34
	v_mov_b32_e32 v14, v34
	v_mov_b32_e32 v15, v34
	v_mov_b32_e32 v16, v34
	v_mov_b32_e32 v17, v34
	v_mov_b32_e32 v26, v34
	v_mov_b32_e32 v27, v34
	v_mov_b32_e32 v28, v34
	v_mov_b32_e32 v29, v34
	v_mov_b32_e32 v30, v34
	v_mov_b32_e32 v31, v34
	v_mov_b32_e32 v32, v34
	v_mov_b32_e32 v33, v34
	v_mov_b32_e32 v42, v34
	v_mov_b32_e32 v43, v34
	v_mov_b32_e32 v44, v34
	v_mov_b32_e32 v45, v34
	v_mov_b32_e32 v46, v34
	v_mov_b32_e32 v47, v34
	v_mov_b32_e32 v48, v34
	v_mov_b32_e32 v49, v34
	v_mov_b32_e32 v58, v34
	v_mov_b32_e32 v59, v34
	v_mov_b32_e32 v60, v34
	v_mov_b32_e32 v61, v34
	v_mov_b32_e32 v62, v34
	v_mov_b32_e32 v63, v34
	v_mov_b32_e32 v64, v34
	v_mov_b32_e32 v65, v34
	v_mov_b32_e32 v66, v34
	v_mov_b32_e32 v67, v34
	v_mov_b32_e32 v68, v34
	v_mov_b32_e32 v69, v34
	v_mov_b32_e32 v70, v34
	v_mov_b32_e32 v71, v34
	v_mov_b32_e32 v72, v34
	v_mov_b32_e32 v73, v34
	v_mov_b32_e32 v82, v34
	v_mov_b32_e32 v83, v34
	v_mov_b32_e32 v84, v34
	v_mov_b32_e32 v85, v34
	v_mov_b32_e32 v86, v34
	v_mov_b32_e32 v87, v34
	v_mov_b32_e32 v88, v34
	v_mov_b32_e32 v89, v34
	v_mov_b32_e32 v98, v34
	v_mov_b32_e32 v99, v34
	v_mov_b32_e32 v100, v34
	v_mov_b32_e32 v101, v34
	v_mov_b32_e32 v102, v34
	v_mov_b32_e32 v103, v34
	v_mov_b32_e32 v104, v34
	v_mov_b32_e32 v105, v34
	v_mov_b32_e32 v114, v34
	v_mov_b32_e32 v115, v34
	v_mov_b32_e32 v116, v34
	v_mov_b32_e32 v117, v34
	v_mov_b32_e32 v118, v34
	v_mov_b32_e32 v119, v34
	v_mov_b32_e32 v120, v34
	v_mov_b32_e32 v121, v34
	v_mov_b32_e32 v74, v34
	v_mov_b32_e32 v75, v34
	v_mov_b32_e32 v76, v34
	v_mov_b32_e32 v77, v34
	v_mov_b32_e32 v78, v34
	v_mov_b32_e32 v79, v34
	v_mov_b32_e32 v80, v34
	v_mov_b32_e32 v81, v34
	v_mov_b32_e32 v90, v34
	v_mov_b32_e32 v91, v34
	v_mov_b32_e32 v92, v34
	v_mov_b32_e32 v93, v34
	v_mov_b32_e32 v94, v34
	v_mov_b32_e32 v95, v34
	v_mov_b32_e32 v96, v34
	v_mov_b32_e32 v97, v34
	v_mov_b32_e32 v106, v34
	v_mov_b32_e32 v107, v34
	v_mov_b32_e32 v108, v34
	v_mov_b32_e32 v109, v34
	v_mov_b32_e32 v110, v34
	v_mov_b32_e32 v111, v34
	v_mov_b32_e32 v112, v34
	v_mov_b32_e32 v113, v34
	v_mov_b32_e32 v122, v34
	v_mov_b32_e32 v123, v34
	v_mov_b32_e32 v124, v34
	v_mov_b32_e32 v125, v34
	v_mov_b32_e32 v126, v34
	v_mov_b32_e32 v127, v34
	v_mov_b32_e32 v128, v34
	v_mov_b32_e32 v129, v34
	v_mov_b32_e32 v18, v34
	v_mov_b32_e32 v19, v34
	v_mov_b32_e32 v20, v34
	v_mov_b32_e32 v21, v34
	v_mov_b32_e32 v22, v34
	v_mov_b32_e32 v23, v34
	v_mov_b32_e32 v24, v34
	v_mov_b32_e32 v25, v34
	v_mov_b32_e32 v2, v34
	v_mov_b32_e32 v3, v34
	v_mov_b32_e32 v4, v34
	v_mov_b32_e32 v5, v34
	v_mov_b32_e32 v6, v34
	v_mov_b32_e32 v7, v34
	v_mov_b32_e32 v8, v34
	v_mov_b32_e32 v9, v34
	.p2align 6

.LBB0_533:
	s_ashr_i32 s25, s24, 31
	s_lshl_b64 s[26:27], s[24:25], 20
	s_add_u32 s26, s1, s26
	s_addc_u32 s27, s33, s27
	s_and_b64 s[28:29], s[2:3], exec
	s_cselect_b32 s25, s27, s35
	s_cselect_b32 s70, s26, s34
	s_ashr_i32 s23, s22, 31
	s_lshl_b64 s[28:29], s[22:23], 20
	s_add_u32 s28, s40, s28
	s_addc_u32 s29, s41, s29
	s_and_b64 s[38:39], s[2:3], exec
	s_cselect_b32 s23, s29, s37
	s_cselect_b32 s71, s28, s36
	s_add_u32 s34, s34, 0x80
	s_addc_u32 s35, s35, 0
	s_add_u32 s72, s36, 0x100
	v_mov_b32_e32 v10, 0
	s_addc_u32 s73, s37, 0
	s_mov_b32 s74, -2
	v_mov_b32_e32 v11, v10
	v_mov_b32_e32 v12, v10
	v_mov_b32_e32 v13, v10
	v_mov_b32_e32 v18, v10
	v_mov_b32_e32 v19, v10
	v_mov_b32_e32 v20, v10
	v_mov_b32_e32 v21, v10
	v_mov_b32_e32 v30, v10
	v_mov_b32_e32 v31, v10
	v_mov_b32_e32 v32, v10
	v_mov_b32_e32 v33, v10
	v_mov_b32_e32 v42, v10
	v_mov_b32_e32 v43, v10
	v_mov_b32_e32 v44, v10
	v_mov_b32_e32 v45, v10
	v_mov_b32_e32 v2, v10
	v_mov_b32_e32 v3, v10
	v_mov_b32_e32 v4, v10
	v_mov_b32_e32 v5, v10
	v_mov_b32_e32 v6, v10
	v_mov_b32_e32 v7, v10
	v_mov_b32_e32 v8, v10
	v_mov_b32_e32 v9, v10
	v_mov_b32_e32 v14, v10
	v_mov_b32_e32 v15, v10
	v_mov_b32_e32 v16, v10
	v_mov_b32_e32 v17, v10
	v_mov_b32_e32 v22, v10
	v_mov_b32_e32 v23, v10
	v_mov_b32_e32 v24, v10
	v_mov_b32_e32 v25, v10
	v_mov_b32_e32 v38, v10
	v_mov_b32_e32 v39, v10
	v_mov_b32_e32 v40, v10
	v_mov_b32_e32 v41, v10
	v_mov_b32_e32 v46, v10
	v_mov_b32_e32 v47, v10
	v_mov_b32_e32 v48, v10
	v_mov_b32_e32 v49, v10
	v_mov_b32_e32 v58, v10
	v_mov_b32_e32 v59, v10
	v_mov_b32_e32 v60, v10
	v_mov_b32_e32 v61, v10
	v_mov_b32_e32 v62, v10
	v_mov_b32_e32 v63, v10
	v_mov_b32_e32 v64, v10
	v_mov_b32_e32 v65, v10
	v_mov_b32_e32 v66, v10
	v_mov_b32_e32 v67, v10
	v_mov_b32_e32 v68, v10
	v_mov_b32_e32 v69, v10
	v_mov_b32_e32 v70, v10
	v_mov_b32_e32 v71, v10
	v_mov_b32_e32 v72, v10
	v_mov_b32_e32 v73, v10
	v_mov_b32_e32 v74, v10
	v_mov_b32_e32 v75, v10
	v_mov_b32_e32 v76, v10
	v_mov_b32_e32 v77, v10
	v_mov_b32_e32 v82, v10
	v_mov_b32_e32 v83, v10
	v_mov_b32_e32 v84, v10
	v_mov_b32_e32 v85, v10
	v_mov_b32_e32 v90, v10
	v_mov_b32_e32 v91, v10
	v_mov_b32_e32 v92, v10
	v_mov_b32_e32 v93, v10
	v_mov_b32_e32 v98, v10
	v_mov_b32_e32 v99, v10
	v_mov_b32_e32 v100, v10
	v_mov_b32_e32 v101, v10
	v_mov_b32_e32 v106, v10
	v_mov_b32_e32 v107, v10
	v_mov_b32_e32 v108, v10
	v_mov_b32_e32 v109, v10
	v_mov_b32_e32 v114, v10
	v_mov_b32_e32 v115, v10
	v_mov_b32_e32 v116, v10
	v_mov_b32_e32 v117, v10
	v_mov_b32_e32 v78, v10
	v_mov_b32_e32 v79, v10
	v_mov_b32_e32 v80, v10
	v_mov_b32_e32 v81, v10
	v_mov_b32_e32 v86, v10
	v_mov_b32_e32 v87, v10
	v_mov_b32_e32 v88, v10
	v_mov_b32_e32 v89, v10
	v_mov_b32_e32 v94, v10
	v_mov_b32_e32 v95, v10
	v_mov_b32_e32 v96, v10
	v_mov_b32_e32 v97, v10
	v_mov_b32_e32 v102, v10
	v_mov_b32_e32 v103, v10
	v_mov_b32_e32 v104, v10
	v_mov_b32_e32 v105, v10
	v_mov_b32_e32 v110, v10
	v_mov_b32_e32 v111, v10
	v_mov_b32_e32 v112, v10
	v_mov_b32_e32 v113, v10
	v_mov_b32_e32 v118, v10
	v_mov_b32_e32 v119, v10
	v_mov_b32_e32 v120, v10
	v_mov_b32_e32 v121, v10
	v_mov_b32_e32 v122, v10
	v_mov_b32_e32 v123, v10
	v_mov_b32_e32 v124, v10
	v_mov_b32_e32 v125, v10
	v_mov_b32_e32 v126, v10
	v_mov_b32_e32 v127, v10
	v_mov_b32_e32 v128, v10
	v_mov_b32_e32 v129, v10
	v_mov_b32_e32 v54, v10
	v_mov_b32_e32 v55, v10
	v_mov_b32_e32 v56, v10
	v_mov_b32_e32 v57, v10
	v_mov_b32_e32 v50, v10
	v_mov_b32_e32 v51, v10
	v_mov_b32_e32 v52, v10
	v_mov_b32_e32 v53, v10
	v_mov_b32_e32 v34, v10
	v_mov_b32_e32 v35, v10
	v_mov_b32_e32 v36, v10
	v_mov_b32_e32 v37, v10
	v_mov_b32_e32 v26, v10
	v_mov_b32_e32 v27, v10
	v_mov_b32_e32 v28, v10
	v_mov_b32_e32 v29, v10
	.p2align 6

.LBB0_726:
	v_mov_b32_e32 v173, v169
	v_mov_b32_e32 v175, v169
	s_add_u32 s31, s40, 0x100
	v_mov_b32_e32 v34, 0
	v_lshl_add_u64 v[176:177], s[26:27], 0, v[174:175]
	v_lshl_add_u64 v[178:179], s[26:27], 0, v[172:173]
	s_addc_u32 s35, s41, 0
	s_mov_b32 s81, -2
	s_mov_b64 s[40:41], 0
	v_mov_b32_e32 v35, v34
	v_mov_b32_e32 v36, v34
	v_mov_b32_e32 v37, v34
	v_mov_b32_e32 v42, v34
	v_mov_b32_e32 v43, v34
	v_mov_b32_e32 v44, v34
	v_mov_b32_e32 v45, v34
	v_mov_b32_e32 v50, v34
	v_mov_b32_e32 v51, v34
	v_mov_b32_e32 v52, v34
	v_mov_b32_e32 v53, v34
	v_mov_b32_e32 v58, v34
	v_mov_b32_e32 v59, v34
	v_mov_b32_e32 v60, v34
	v_mov_b32_e32 v61, v34
	v_mov_b32_e32 v66, v34
	v_mov_b32_e32 v67, v34
	v_mov_b32_e32 v68, v34
	v_mov_b32_e32 v69, v34
	v_mov_b32_e32 v74, v34
	v_mov_b32_e32 v75, v34
	v_mov_b32_e32 v76, v34
	v_mov_b32_e32 v77, v34
	v_mov_b32_e32 v82, v34
	v_mov_b32_e32 v83, v34
	v_mov_b32_e32 v84, v34
	v_mov_b32_e32 v85, v34
	v_mov_b32_e32 v90, v34
	v_mov_b32_e32 v91, v34
	v_mov_b32_e32 v92, v34
	v_mov_b32_e32 v93, v34
	v_mov_b32_e32 v38, v34
	v_mov_b32_e32 v39, v34
	v_mov_b32_e32 v40, v34
	v_mov_b32_e32 v41, v34
	v_mov_b32_e32 v46, v34
	v_mov_b32_e32 v47, v34
	v_mov_b32_e32 v48, v34
	v_mov_b32_e32 v49, v34
	v_mov_b32_e32 v54, v34
	v_mov_b32_e32 v55, v34
	v_mov_b32_e32 v56, v34
	v_mov_b32_e32 v57, v34
	v_mov_b32_e32 v62, v34
	v_mov_b32_e32 v63, v34
	v_mov_b32_e32 v64, v34
	v_mov_b32_e32 v65, v34
	v_mov_b32_e32 v70, v34
	v_mov_b32_e32 v71, v34
	v_mov_b32_e32 v72, v34
	v_mov_b32_e32 v73, v34
	v_mov_b32_e32 v78, v34
	v_mov_b32_e32 v79, v34
	v_mov_b32_e32 v80, v34
	v_mov_b32_e32 v81, v34
	v_mov_b32_e32 v86, v34
	v_mov_b32_e32 v87, v34
	v_mov_b32_e32 v88, v34
	v_mov_b32_e32 v89, v34
	v_mov_b32_e32 v94, v34
	v_mov_b32_e32 v95, v34
	v_mov_b32_e32 v96, v34
	v_mov_b32_e32 v97, v34
	v_mov_b32_e32 v98, v34
	v_mov_b32_e32 v99, v34
	v_mov_b32_e32 v100, v34
	v_mov_b32_e32 v101, v34
	v_mov_b32_e32 v106, v34
	v_mov_b32_e32 v107, v34
	v_mov_b32_e32 v108, v34
	v_mov_b32_e32 v109, v34
	v_mov_b32_e32 v114, v34
	v_mov_b32_e32 v115, v34
	v_mov_b32_e32 v116, v34
	v_mov_b32_e32 v117, v34
	v_mov_b32_e32 v122, v34
	v_mov_b32_e32 v123, v34
	v_mov_b32_e32 v124, v34
	v_mov_b32_e32 v125, v34
	v_mov_b32_e32 v130, v34
	v_mov_b32_e32 v131, v34
	v_mov_b32_e32 v132, v34
	v_mov_b32_e32 v133, v34
	v_mov_b32_e32 v138, v34
	v_mov_b32_e32 v139, v34
	v_mov_b32_e32 v140, v34
	v_mov_b32_e32 v141, v34
	v_mov_b32_e32 v146, v34
	v_mov_b32_e32 v147, v34
	v_mov_b32_e32 v148, v34
	v_mov_b32_e32 v149, v34
	v_mov_b32_e32 v154, v34
	v_mov_b32_e32 v155, v34
	v_mov_b32_e32 v156, v34
	v_mov_b32_e32 v157, v34
	v_mov_b32_e32 v102, v34
	v_mov_b32_e32 v103, v34
	v_mov_b32_e32 v104, v34
	v_mov_b32_e32 v105, v34
	v_mov_b32_e32 v110, v34
	v_mov_b32_e32 v111, v34
	v_mov_b32_e32 v112, v34
	v_mov_b32_e32 v113, v34
	v_mov_b32_e32 v118, v34
	v_mov_b32_e32 v119, v34
	v_mov_b32_e32 v120, v34
	v_mov_b32_e32 v121, v34
	v_mov_b32_e32 v126, v34
	v_mov_b32_e32 v127, v34
	v_mov_b32_e32 v128, v34
	v_mov_b32_e32 v129, v34
	v_mov_b32_e32 v134, v34
	v_mov_b32_e32 v135, v34
	v_mov_b32_e32 v136, v34
	v_mov_b32_e32 v137, v34
	v_mov_b32_e32 v142, v34
	v_mov_b32_e32 v143, v34
	v_mov_b32_e32 v144, v34
	v_mov_b32_e32 v145, v34
	v_mov_b32_e32 v150, v34
	v_mov_b32_e32 v151, v34
	v_mov_b32_e32 v152, v34
	v_mov_b32_e32 v153, v34
	v_mov_b32_e32 v158, v34
	v_mov_b32_e32 v159, v34
	v_mov_b32_e32 v160, v34
	v_mov_b32_e32 v161, v34
	.p2align 6

.LBB0_830:
	s_ashr_i32 s39, s38, 31
	s_lshl_b64 s[44:45], s[38:39], 19
	s_add_u32 s44, s1, s44
	s_addc_u32 s45, s29, s45
	s_and_b64 s[66:67], s[66:67], exec
	s_cselect_b32 s17, s45, s63
	s_cselect_b32 s39, s44, s62
	s_add_u32 s62, s62, 0x80
	s_addc_u32 s63, s63, 0
	s_add_u32 s41, s64, 0x100
	v_mov_b32_e32 v46, 0
	s_addc_u32 s90, s65, 0
	s_mov_b32 s91, -2
	v_mov_b32_e32 v47, v46
	v_mov_b32_e32 v48, v46
	v_mov_b32_e32 v49, v46
	v_mov_b32_e32 v62, v46
	v_mov_b32_e32 v63, v46
	v_mov_b32_e32 v64, v46
	v_mov_b32_e32 v65, v46
	v_mov_b32_e32 v78, v46
	v_mov_b32_e32 v79, v46
	v_mov_b32_e32 v80, v46
	v_mov_b32_e32 v81, v46
	v_mov_b32_e32 v86, v46
	v_mov_b32_e32 v87, v46
	v_mov_b32_e32 v88, v46
	v_mov_b32_e32 v89, v46
	v_mov_b32_e32 v34, v46
	v_mov_b32_e32 v35, v46
	v_mov_b32_e32 v36, v46
	v_mov_b32_e32 v37, v46
	v_mov_b32_e32 v38, v46
	v_mov_b32_e32 v39, v46
	v_mov_b32_e32 v40, v46
	v_mov_b32_e32 v41, v46
	v_mov_b32_e32 v42, v46
	v_mov_b32_e32 v43, v46
	v_mov_b32_e32 v44, v46
	v_mov_b32_e32 v45, v46
	v_mov_b32_e32 v58, v46
	v_mov_b32_e32 v59, v46
	v_mov_b32_e32 v60, v46
	v_mov_b32_e32 v61, v46
	v_mov_b32_e32 v70, v46
	v_mov_b32_e32 v71, v46
	v_mov_b32_e32 v72, v46
	v_mov_b32_e32 v73, v46
	v_mov_b32_e32 v82, v46
	v_mov_b32_e32 v83, v46
	v_mov_b32_e32 v84, v46
	v_mov_b32_e32 v85, v46
	v_mov_b32_e32 v90, v46
	v_mov_b32_e32 v91, v46
	v_mov_b32_e32 v92, v46
	v_mov_b32_e32 v93, v46
	v_mov_b32_e32 v94, v46
	v_mov_b32_e32 v95, v46
	v_mov_b32_e32 v96, v46
	v_mov_b32_e32 v97, v46
	v_mov_b32_e32 v98, v46
	v_mov_b32_e32 v99, v46
	v_mov_b32_e32 v100, v46
	v_mov_b32_e32 v101, v46
	v_mov_b32_e32 v102, v46
	v_mov_b32_e32 v103, v46
	v_mov_b32_e32 v104, v46
	v_mov_b32_e32 v105, v46
	v_mov_b32_e32 v110, v46
	v_mov_b32_e32 v111, v46
	v_mov_b32_e32 v112, v46
	v_mov_b32_e32 v113, v46
	v_mov_b32_e32 v118, v46
	v_mov_b32_e32 v119, v46
	v_mov_b32_e32 v120, v46
	v_mov_b32_e32 v121, v46
	v_mov_b32_e32 v126, v46
	v_mov_b32_e32 v127, v46
	v_mov_b32_e32 v128, v46
	v_mov_b32_e32 v129, v46
	v_mov_b32_e32 v134, v46
	v_mov_b32_e32 v135, v46
	v_mov_b32_e32 v136, v46
	v_mov_b32_e32 v137, v46
	v_mov_b32_e32 v142, v46
	v_mov_b32_e32 v143, v46
	v_mov_b32_e32 v144, v46
	v_mov_b32_e32 v145, v46
	v_mov_b32_e32 v150, v46
	v_mov_b32_e32 v151, v46
	v_mov_b32_e32 v152, v46
	v_mov_b32_e32 v153, v46
	v_mov_b32_e32 v106, v46
	v_mov_b32_e32 v107, v46
	v_mov_b32_e32 v108, v46
	v_mov_b32_e32 v109, v46
	v_mov_b32_e32 v114, v46
	v_mov_b32_e32 v115, v46
	v_mov_b32_e32 v116, v46
	v_mov_b32_e32 v117, v46
	v_mov_b32_e32 v122, v46
	v_mov_b32_e32 v123, v46
	v_mov_b32_e32 v124, v46
	v_mov_b32_e32 v125, v46
	v_mov_b32_e32 v130, v46
	v_mov_b32_e32 v131, v46
	v_mov_b32_e32 v132, v46
	v_mov_b32_e32 v133, v46
	v_mov_b32_e32 v138, v46
	v_mov_b32_e32 v139, v46
	v_mov_b32_e32 v140, v46
	v_mov_b32_e32 v141, v46
	v_mov_b32_e32 v146, v46
	v_mov_b32_e32 v147, v46
	v_mov_b32_e32 v148, v46
	v_mov_b32_e32 v149, v46
	v_mov_b32_e32 v154, v46
	v_mov_b32_e32 v155, v46
	v_mov_b32_e32 v156, v46
	v_mov_b32_e32 v157, v46
	v_mov_b32_e32 v158, v46
	v_mov_b32_e32 v159, v46
	v_mov_b32_e32 v160, v46
	v_mov_b32_e32 v161, v46
	v_mov_b32_e32 v74, v46
	v_mov_b32_e32 v75, v46
	v_mov_b32_e32 v76, v46
	v_mov_b32_e32 v77, v46
	v_mov_b32_e32 v66, v46
	v_mov_b32_e32 v67, v46
	v_mov_b32_e32 v68, v46
	v_mov_b32_e32 v69, v46
	v_mov_b32_e32 v54, v46
	v_mov_b32_e32 v55, v46
	v_mov_b32_e32 v56, v46
	v_mov_b32_e32 v57, v46
	v_mov_b32_e32 v50, v46
	v_mov_b32_e32 v51, v46
	v_mov_b32_e32 v52, v46
	v_mov_b32_e32 v53, v46
	.p2align 6
